# NA mask branch-free rewrite + attnA: K-frag preload, MFMA/VALU interleave, batched ConvW finish LDS reads, trimmed rescale check
# speedup vs baseline: 1.0370x; 1.0312x over previous
.LBB0_411:
	s_and_b64 s[62:63], s[28:29], s[4:5]
	s_mul_hi_i32 s5, s56, s46
	s_mul_i32 s4, s56, s46
	s_xor_b64 s[60:61], s[62:63], -1
	s_ashr_i32 s47, s46, 31
	s_lshl_b64 s[4:5], s[4:5], 2
	s_waitcnt lgkmcnt(0)
	s_add_u32 s1, s14, s4
	s_addc_u32 s8, s15, s5
	s_ashr_i32 s11, s10, 31
	s_lshl_b64 s[4:5], s[10:11], 2
	s_add_u32 s58, s1, s4
	s_addc_u32 s59, s8, s5
	s_lshl_b32 s1, s26, 3
	s_add_i32 s4, s1, s33
	s_ashr_i32 s5, s4, 31
	s_ashr_i32 s31, s30, 31
	s_lshl_b64 s[4:5], s[4:5], 21
	s_lshl_b64 s[10:11], s[30:31], 15
	s_add_u32 s1, s73, s4
	s_addc_u32 s4, s75, s5
	v_mbcnt_lo_u32_b32 v9, -1, 0
	v_mbcnt_hi_u32_b32 v9, -1, v9
	v_readlane_b32 s18, v252, 13
	v_and_b32_e32 v8, 31, v9
	s_add_u32 s10, s1, s10
	v_or_b32_e32 v166, s18, v8
	s_addc_u32 s11, s4, s11
	v_lshlrev_b64 v[0:1], 7, v[166:167]
	v_and_b32_e32 v2, 0xffffffe0, v9
	v_lshl_add_u64 v[0:1], s[10:11], 0, v[0:1]
	v_ashrrev_i32_e32 v3, 31, v2
	v_lshl_add_u64 v[10:11], v[0:1], 0, v[2:3]
	global_load_dwordx4 v[4:7], v[10:11], off offset:16
	global_load_dwordx4 v[182:185], v[10:11], off
	global_load_dwordx4 v[0:3], v[10:11], off offset:80
	global_load_dwordx4 v[176:179], v[10:11], off offset:64
	v_ashrrev_i32_e32 v48, 3, v9
	s_lshl_b32 s1, s26, 1
	s_ashr_i32 s4, s33, 2
	s_waitcnt vmcnt(1)
	v_add_u32_e32 v2, s84, v48
	s_add_i32 s4, s1, s4
	v_lshrrev_b32_e32 v3, 1, v2
	s_ashr_i32 s5, s4, 31
	v_xor_b32_e32 v3, v3, v9
	s_lshl_b64 s[4:5], s[4:5], 21
	v_lshlrev_b32_e32 v3, 4, v3
	s_add_u32 s14, s80, s4
	v_and_b32_e32 v51, 0x70, v3
	v_lshlrev_b32_e32 v3, 4, v9
	v_mov_b32_e32 v166, v167
	s_addc_u32 s15, s81, s5
	v_and_b32_e32 v6, 0xffffffc0, v3
	v_mov_b32_e32 v163, v160
	v_mov_b32_e32 v164, v161
	v_mov_b32_e32 v165, v162
	v_mov_b64_e32 v[174:175], v[166:167]
	s_mov_b32 m0, s89
	s_add_u32 s16, s82, s4
	v_lshl_or_b32 v2, v2, 7, v51
	v_add_u32_e32 v49, s85, v6
	v_bitop3_b32 v50, v3, 48, v9 bitop3:0x48
	v_mov_b64_e32 v[172:173], v[164:165]
	v_mov_b64_e32 v[170:171], v[162:163]
	v_mov_b64_e32 v[168:169], v[160:161]
	v_mov_b32_e32 v3, v167
	s_addc_u32 s17, s83, s5
	v_or_b32_e32 v6, v49, v50
	v_lshl_add_u64 v[10:11], s[14:15], 0, v[2:3]
	global_load_lds_dwordx4 v2, s[14:15]
	v_mov_b32_e32 v7, v167
	s_add_i32 m0, s89, 0x6000
	v_lshl_add_u64 v[2:3], s[16:17], 0, v[6:7]
	global_load_lds_dwordx4 v6, s[16:17]
	v_lshl_add_u64 v[6:7], v[10:11], 0, s[6:7]
	s_add_i32 m0, s89, 0x2000
	v_lshl_add_u64 v[2:3], v[2:3], 0, s[6:7]
	global_load_lds_dwordx4 v[6:7], off
	s_add_i32 m0, s89, 0x8000
	s_and_b64 vcc, exec, s[60:61]
	global_load_lds_dwordx4 v[2:3], off
	v_lshl_add_u64 v[228:229], v[6:7], 0, s[6:7]
	s_add_i32 m0, s89, 0x4000
	s_nop 0
	global_load_lds_dwordx4 v[228:229], off
	v_readlane_b32 s19, v252, 14
	s_cbranch_vccnz .LBB0_413
	v_mbcnt_lo_u32_b32 v6, -1, 0
	v_mbcnt_hi_u32_b32 v6, -1, v6
	s_mov_b32 m0, s87
	v_ashrrev_i32_e32 v2, 3, v6
	v_mad_i64_i32 v[2:3], s[10:11], s56, v2, 0
	v_lshlrev_b32_e32 v6, 4, v6
	v_lshl_add_u64 v[2:3], v[2:3], 2, s[58:59]
	v_and_b32_e32 v166, 0x70, v6
	v_lshl_add_u64 v[2:3], v[2:3], 0, v[166:167]
	global_load_lds_dwordx4 v[2:3], off nt
.LBB0_413:
	v_bfe_u32 v3, v9, 1, 3
	v_ashrrev_i32_e32 v7, 4, v9
	v_lshlrev_b32_e32 v6, 7, v8
	v_and_b32_e32 v10, -2, v7
	v_bitop3_b32 v11, v7, v3, -2 bitop3:0x6c
	v_bitop3_b32 v3, v7, v3, 1 bitop3:0x36
	v_lshrrev_b32_e32 v2, 1, v9
	v_lshl_add_u32 v224, v3, 4, v6
	v_add_u32_e32 v3, 4, v10
	v_bitop3_b32 v3, v3, v2, 7 bitop3:0x78
	v_lshl_add_u32 v221, v3, 4, v6
	v_add_u32_e32 v3, 5, v10
	v_bitop3_b32 v2, v3, v2, 7 bitop3:0x78
	v_lshl_add_u32 v222, v2, 4, v6
	v_bfe_u32 v2, v9, 2, 2
	v_lshl_add_u32 v223, v11, 4, v6
	v_lshlrev_b32_e32 v3, 6, v8
	v_bitop3_b32 v6, v7, v2, -2 bitop3:0x6c
	v_bitop3_b32 v2, v7, v2, 1 bitop3:0x36
	v_lshl_add_u32 v220, v2, 4, v3
	s_waitcnt vmcnt(0)
	s_barrier
	v_add_u32_e32 v2, 0, v223
	v_lshl_add_u32 v163, v6, 4, v3
	v_add_u32_e32 v3, 0, v224
	ds_read_b128 v[6:9], v2
	ds_read_b64 v[10:11], v3
	v_mov_b32_e32 v186, v4
	v_mov_b32_e32 v187, v5
	ds_read_b128 v[12:15], v2 offset:4096
	ds_read_b64 v[16:17], v3 offset:4096
	s_waitcnt lgkmcnt(0)
	v_mfma_scale_f32_32x32x64_f8f6f4 v[32:47], v[6:11], v[182:187], 0, v217, v216 op_sel_hi:[0,0,0] cbsz:2 blgp:2
	v_mov_b32_e32 v180, v0
	v_add_u32_e32 v2, 0, v221
	v_add_u32_e32 v3, 0, v222
	ds_read_b128 v[52:55], v2
	ds_read_b64 v[56:57], v3
	v_mov_b32_e32 v181, v1
	ds_read_b128 v[58:61], v2 offset:4096
	ds_read_b64 v[62:63], v3 offset:4096
	s_waitcnt vmcnt(0) lgkmcnt(0)
	v_mfma_scale_f32_32x32x64_f8f6f4 v[32:47], v[52:57], v[176:181], v[32:47], v217, v216 op_sel_hi:[0,0,0] cbsz:2 blgp:2
	s_cmp_lg_u64 s[12:13], 0
	s_cselect_b64 s[54:55], -1, 0
	s_cmp_lt_u32 s0, 2
	s_mov_b32 s0, 0x3f400000
	s_cselect_b64 s[52:53], -1, 0
	s_mov_b32 s8, s9
	v_mfma_scale_f32_32x32x64_f8f6f4 v[16:31], v[12:17], v[182:187], 0, v217, v216 op_sel_hi:[0,0,0] cbsz:2 blgp:2
	s_nop 4
	v_max_f32_e32 v52, v33, v33
	v_max_f32_e32 v53, v32, v32
	v_max_f32_e32 v52, v53, v52
	v_max3_f32 v52, v52, v34, v35
	v_max3_f32 v52, v52, v36, v37
	v_max3_f32 v52, v52, v38, v39
	v_max3_f32 v52, v52, v40, v41
	v_mfma_scale_f32_32x32x64_f8f6f4 v[16:31], v[58:63], v[176:181], v[16:31], v217, v216 op_sel_hi:[0,0,0] cbsz:2 blgp:2
	v_max3_f32 v52, v52, v42, v43
	v_max3_f32 v52, v52, v44, v45
	v_max3_f32 v52, v52, v46, v47
	s_mov_b32 s10, s9
	s_mov_b32 s11, s9
	s_mov_b32 s12, s9
	s_mov_b32 s13, s9
	s_nop 4
	v_max3_f32 v52, v52, v16, v17
	v_max3_f32 v52, v52, v18, v19
	v_max3_f32 v52, v52, v20, v21
	v_max3_f32 v52, v52, v22, v23
	v_max3_f32 v52, v52, v24, v25
	v_max3_f32 v52, v52, v26, v27
	v_max3_f32 v52, v52, v28, v29
	v_max3_f32 v52, v52, v30, v31
	v_mov_b32_e32 v53, v52
	s_nop 1
	v_permlane32_swap_b32_e32 v52, v53
	v_max_f32_e32 v53, v53, v53
	v_max_f32_e32 v52, v52, v52
	v_max_f32_e32 v52, v52, v53
	v_add_f32_e32 v53, 0x7149f2ca, v52
	v_cmp_ge_f32_e32 vcc, s0, v53
	v_max_f32_e32 v52, 0xf149f2ca, v52
	s_cmp_lg_u64 vcc, exec
	v_add_f32_e32 v52, 2.0, v52
	s_cselect_b64 vcc, -1, 0
	v_cndmask_b32_e32 v52, v219, v52, vcc
	v_add_f32_e32 v53, -4.0, v52
	s_lshl_b32 s0, s46, 2
	v_sub_f32_e32 v32, v32, v53
	v_sub_f32_e32 v33, v33, v53
	v_sub_f32_e32 v34, v34, v53
	v_sub_f32_e32 v35, v35, v53
	v_sub_f32_e32 v36, v36, v53
	v_sub_f32_e32 v37, v37, v53
	v_sub_f32_e32 v38, v38, v53
	v_sub_f32_e32 v39, v39, v53
	v_sub_f32_e32 v40, v40, v53
	v_sub_f32_e32 v41, v41, v53
	v_sub_f32_e32 v42, v42, v53
	v_sub_f32_e32 v43, v43, v53
	v_sub_f32_e32 v44, v44, v53
	v_sub_f32_e32 v45, v45, v53
	v_sub_f32_e32 v46, v46, v53
	v_sub_f32_e32 v47, v47, v53
	s_add_i32 s0, s0, 0
	s_mov_b32 s14, s9
	s_mov_b32 s15, s9
	s_mov_b32 s16, s9
	s_mov_b32 s17, s9
	s_mov_b32 s18, s9
	s_mov_b32 s19, s9
	s_mov_b32 s20, s9
	s_mov_b32 s21, s9
	s_mov_b32 s22, s9
	s_mov_b32 s23, s9
	v_mov_b64_e32 v[0:1], s[8:9]
	v_exp_f32_e32 v144, v32
	v_exp_f32_e32 v145, v33
	v_exp_f32_e32 v146, v34
	v_exp_f32_e32 v147, v35
	v_exp_f32_e32 v148, v36
	v_exp_f32_e32 v149, v37
	v_exp_f32_e32 v150, v38
	v_exp_f32_e32 v151, v39
	v_exp_f32_e32 v152, v40
	v_exp_f32_e32 v153, v41
	v_exp_f32_e32 v154, v42
	v_exp_f32_e32 v155, v43
	v_exp_f32_e32 v156, v44
	v_exp_f32_e32 v157, v45
	v_exp_f32_e32 v158, v46
	v_exp_f32_e32 v159, v47
	s_add_i32 s0, s0, 0x1c800
	v_mov_b64_e32 v[2:3], s[10:11]
	v_mov_b64_e32 v[4:5], s[12:13]
	v_mov_b64_e32 v[6:7], s[14:15]
	v_mov_b64_e32 v[8:9], s[16:17]
	v_mov_b64_e32 v[10:11], s[18:19]
	v_mov_b64_e32 v[12:13], s[20:21]
	v_mov_b64_e32 v[14:15], s[22:23]
	v_sub_f32_e32 v128, v16, v53
	s_and_b64 s[10:11], s[52:53], exec
	v_lshlrev_b32_e32 v16, 7, v48
	v_sub_f32_e32 v80, 4.0, v52
	v_sub_f32_e32 v143, v31, v53
	v_sub_f32_e32 v142, v30, v53
	v_sub_f32_e32 v141, v29, v53
	v_sub_f32_e32 v140, v28, v53
	v_sub_f32_e32 v139, v27, v53
	v_sub_f32_e32 v138, v26, v53
	v_sub_f32_e32 v137, v25, v53
	v_sub_f32_e32 v136, v24, v53
	v_sub_f32_e32 v135, v23, v53
	v_sub_f32_e32 v134, v22, v53
	v_sub_f32_e32 v133, v21, v53
	v_sub_f32_e32 v132, v20, v53
	v_sub_f32_e32 v131, v19, v53
	v_sub_f32_e32 v130, v18, v53
	v_sub_f32_e32 v129, v17, v53
	s_cselect_b32 s14, 23, 22
	v_add3_u32 v164, s85, v16, v51
	s_add_u32 s10, s78, s4
	v_add_u32_e32 v174, v49, v50
	v_mov_b64_e32 v[62:63], v[14:15]
	v_mov_b64_e32 v[46:47], v[14:15]
	v_mov_b64_e32 v[30:31], v[14:15]
	v_mov_b64_e32 v[78:79], v[14:15]
	s_mov_b32 s1, 2
	s_mov_b32 s57, 1
	s_mov_b32 s27, -2
	v_mov_b32_e32 v81, v80
	v_mov_b32_e32 v82, v80
	v_mov_b32_e32 v83, v80
	v_mov_b32_e32 v84, v80
	v_mov_b32_e32 v85, v80
	v_mov_b32_e32 v86, v80
	v_mov_b32_e32 v87, v80
	v_mov_b32_e32 v88, v80
	v_mov_b32_e32 v89, v80
	v_mov_b32_e32 v90, v80
	v_mov_b32_e32 v91, v80
	v_mov_b32_e32 v92, v80
	v_mov_b32_e32 v93, v80
	v_mov_b32_e32 v94, v80
	v_mov_b32_e32 v95, v80
	s_mov_b32 s15, 0
	v_mov_b32_e32 v165, v167
	s_addc_u32 s11, s79, s5
	v_mov_b32_e32 v175, v167
	v_mov_b64_e32 v[60:61], v[12:13]
	v_mov_b64_e32 v[58:59], v[10:11]
	v_mov_b64_e32 v[56:57], v[8:9]
	v_mov_b64_e32 v[54:55], v[6:7]
	v_mov_b64_e32 v[52:53], v[4:5]
	v_mov_b64_e32 v[50:51], v[2:3]
	v_mov_b64_e32 v[48:49], v[0:1]
	v_mov_b64_e32 v[44:45], v[12:13]
	v_mov_b64_e32 v[42:43], v[10:11]
	v_mov_b64_e32 v[40:41], v[8:9]
	v_mov_b64_e32 v[38:39], v[6:7]
	v_mov_b64_e32 v[36:37], v[4:5]
	v_mov_b64_e32 v[34:35], v[2:3]
	v_mov_b64_e32 v[32:33], v[0:1]
	v_mov_b64_e32 v[28:29], v[12:13]
	v_mov_b64_e32 v[26:27], v[10:11]
	v_mov_b64_e32 v[24:25], v[8:9]
	v_mov_b64_e32 v[22:23], v[6:7]
	v_mov_b64_e32 v[20:21], v[4:5]
	v_mov_b64_e32 v[18:19], v[2:3]
	v_mov_b64_e32 v[16:17], v[0:1]
	s_mov_b32 s16, 2
	v_mov_b64_e32 v[76:77], v[12:13]
	v_mov_b64_e32 v[74:75], v[10:11]
	v_mov_b64_e32 v[72:73], v[8:9]
	v_mov_b64_e32 v[70:71], v[6:7]
	v_mov_b64_e32 v[68:69], v[4:5]
	v_mov_b64_e32 v[66:67], v[2:3]
	v_mov_b64_e32 v[64:65], v[0:1]
	ds_read_b128 v[228:231], v223 offset:8192
	ds_read_b64 v[232:233], v224 offset:8192
	ds_read_b128 v[234:237], v223 offset:12288
	ds_read_b64 v[238:239], v224 offset:12288
	ds_read_b128 v[240:243], v221 offset:8192
	ds_read_b64 v[244:245], v222 offset:8192
	ds_read_b128 v[246:249], v221 offset:12288
	ds_read_b64 v[250:251], v222 offset:12288
	s_mov_b64 s[4:5], -1
	s_and_b64 vcc, exec, s[60:61]
	s_cbranch_vccz .LBB0_415

.LBB0_417:
	v_lshl_add_u64 v[212:213], s[10:11], 0, v[164:165]
	s_mov_b64 s[4:5], 0x74006000
	v_lshl_add_u64 v[96:97], v[212:213], 0, s[4:5]
	s_lshl_b32 s4, s16, 13
	s_add_i32 s8, s89, s4
	s_add_i32 s4, s16, 1
	s_cmp_lg_u32 s16, 2
	s_cselect_b32 s4, s4, 0
	s_lshl_b32 s4, s4, 13
	s_add_i32 s4, s89, s4
	s_barrier
	s_mov_b32 m0, s4
	v_lshl_add_u64 v[214:215], s[10:11], 0, v[174:175]
	s_mov_b64 s[4:5], 0x74804000
	global_load_lds_dwordx4 v[96:97], off
	v_lshl_add_u64 v[96:97], v[214:215], 0, s[4:5]
	s_add_i32 m0, s8, 0x6000
	s_andn2_b64 vcc, exec, s[62:63]
	global_load_lds_dwordx4 v[96:97], off
	s_mov_b64 s[4:5], s[60:61]
	s_cbranch_vccnz .LBB0_419
	s_add_i32 s8, s1, -1
	s_and_b32 s17, s8, 7
	s_lshr_b32 s8, s8, 3
	v_mbcnt_lo_u32_b32 v98, -1, 0
	v_mbcnt_hi_u32_b32 v98, -1, v98
	s_lshl_b64 s[12:13], s[8:9], 24
	v_ashrrev_i32_e32 v96, 3, v98
	s_add_u32 s12, s58, s12
	v_lshl_add_u32 v96, s17, 3, v96
	v_add_u32_e32 v98, s27, v98
	s_addc_u32 s13, s59, s13
	v_mad_i64_i32 v[96:97], s[18:19], s56, v96, 0
	v_lshl_add_u32 v98, v98, 4, 16
	s_lshl_b32 s8, s17, 10
	v_lshl_add_u64 v[96:97], v[96:97], 2, s[12:13]
	v_and_b32_e32 v166, 0x70, v98
	s_add_i32 s8, s66, s8
	v_lshl_add_u64 v[96:97], v[96:97], 0, v[166:167]
	s_add_i32 m0, s8, 0xc800
	s_nop 0
	global_load_lds_dwordx4 v[96:97], off nt
.LBB0_419:
	s_lshl_b32 s8, s15, 13
	s_add_i32 s8, s8, 0
	v_add_u32_e32 v225, s8, v163
	v_add_u32_e32 v226, s8, v220
	v_mfma_scale_f32_32x32x64_f8f6f4 v[112:127], v[228:233], v[182:187], v[80:95], v217, v216 op_sel_hi:[0,0,0] cbsz:2 blgp:2
	v_exp_f32_e32 v128, v128
	v_exp_f32_e32 v129, v129
	v_exp_f32_e32 v130, v130
	v_exp_f32_e32 v131, v131
	v_mfma_scale_f32_32x32x64_f8f6f4 v[96:111], v[234:239], v[182:187], v[80:95], v217, v216 op_sel_hi:[0,0,0] cbsz:2 blgp:2
	v_exp_f32_e32 v132, v132
	v_exp_f32_e32 v133, v133
	v_exp_f32_e32 v134, v134
	v_exp_f32_e32 v135, v135
	v_mfma_scale_f32_32x32x64_f8f6f4 v[112:127], v[240:245], v[176:181], v[112:127], v217, v216 op_sel_hi:[0,0,0] cbsz:2 blgp:2
	v_exp_f32_e32 v136, v136
	v_exp_f32_e32 v137, v137
	v_exp_f32_e32 v138, v138
	v_exp_f32_e32 v139, v139
	v_mfma_scale_f32_32x32x64_f8f6f4 v[96:111], v[246:251], v[176:181], v[96:111], v217, v216 op_sel_hi:[0,0,0] cbsz:2 blgp:2
	s_add_i32 s8, s57, 1
	s_cmp_lg_u32 s57, 2
	s_cselect_b32 s8, s8, 0
	s_lshl_b32 s8, s8, 13
	v_add_u32_e32 v200, s8, v223
	v_add_u32_e32 v201, s8, v224
	v_add_u32_e32 v202, s8, v221
	v_add_u32_e32 v203, s8, v222
	ds_read_b128 v[228:231], v200
	ds_read_b64 v[232:233], v201
	ds_read_b128 v[234:237], v200 offset:4096
	ds_read_b64 v[238:239], v201 offset:4096
	ds_read_b128 v[240:243], v202
	ds_read_b64 v[244:245], v203
	ds_read_b128 v[246:249], v202 offset:4096
	ds_read_b64 v[250:251], v203 offset:4096
	ds_read_b128 v[206:209], v225 offset:24576
	ds_read_b64 v[210:211], v226 offset:24576
	ds_read_b128 v[200:203], v225 offset:26624
	ds_read_b64 v[204:205], v226 offset:26624
	ds_read_b128 v[194:197], v225 offset:28672
	ds_read_b64 v[198:199], v226 offset:28672
	ds_read_b128 v[188:191], v225 offset:30720
	ds_read_b64 v[192:193], v226 offset:30720
	v_exp_f32_e32 v140, v140
	v_exp_f32_e32 v141, v141
	v_exp_f32_e32 v142, v142
	v_exp_f32_e32 v143, v143
	s_nop 0
	v_cvt_scalef32_2xpk16_bf6_f32 v[128:133], v[144:159], v[128:143], 1.0
	s_nop 1
	v_mfma_scale_f32_32x32x64_f8f6f4 v[64:79], v[128:133], v[168:173], v[64:79], v218, v218 op_sel_hi:[0,0,0] cbsz:3 blgp:2
	v_max_f32_e32 v225, v113, v113
	v_max_f32_e32 v226, v112, v112
	v_max_f32_e32 v225, v226, v225
	v_max3_f32 v225, v225, v114, v115
	s_waitcnt lgkmcnt(0)
	v_mfma_scale_f32_32x32x64_f8f6f4 v[0:15], v[128:133], v[206:211], v[0:15], v218, v217 op_sel_hi:[0,0,0] cbsz:3 blgp:2
	v_max3_f32 v225, v225, v116, v117
	v_max3_f32 v225, v225, v118, v119
	v_max3_f32 v225, v225, v120, v121
	v_max3_f32 v225, v225, v122, v123
	v_mfma_scale_f32_32x32x64_f8f6f4 v[48:63], v[128:133], v[200:205], v[48:63], v218, v217 op_sel_hi:[0,0,0] cbsz:3 blgp:2
	v_max3_f32 v225, v225, v124, v125
	v_max3_f32 v225, v225, v126, v127
	v_max3_f32 v225, v225, v96, v97
	v_max3_f32 v225, v225, v98, v99
	v_mfma_scale_f32_32x32x64_f8f6f4 v[32:47], v[128:133], v[194:199], v[32:47], v218, v217 op_sel_hi:[0,0,0] cbsz:3 blgp:2
	v_max3_f32 v225, v225, v100, v101
	v_max3_f32 v225, v225, v102, v103
	v_max3_f32 v225, v225, v104, v105
	v_max3_f32 v225, v225, v106, v107
	v_mfma_scale_f32_32x32x64_f8f6f4 v[16:31], v[128:133], v[188:193], v[16:31], v218, v217 op_sel_hi:[0,0,0] cbsz:3 blgp:2
	v_max3_f32 v225, v225, v108, v109
	v_max3_f32 v225, v225, v110, v111
	v_cmp_ge_f32_e32 vcc, s2, v225
	s_cmp_eq_u64 vcc, exec
	s_cbranch_scc0 .LBB0_444
	s_branch .LBB0_424

.LBB0_428:
	s_add_i32 s8, s16, 1
	s_cmp_lg_u32 s16, 2
	s_cselect_b32 s16, s8, 0
	s_lshl_b32 s8, s16, 13
	s_mov_b64 s[12:13], 0x74806000
	s_add_i32 s8, s89, s8
	v_lshl_add_u64 v[128:129], v[214:215], 0, s[12:13]
	s_mov_b64 s[12:13], 0x74008000
	s_barrier
	s_add_i32 s17, s8, 0x6000
	v_lshl_add_u64 v[130:131], v[212:213], 0, s[12:13]
	s_add_i32 s12, s16, 1
	s_cmp_lg_u32 s16, 2
	s_cselect_b32 s12, s12, 0
	s_lshl_b32 s12, s12, 13
	s_add_i32 s12, s89, s12
	s_mov_b32 m0, s12
	s_and_b64 vcc, exec, s[4:5]
	global_load_lds_dwordx4 v[130:131], off
	s_mov_b32 m0, s17
	s_nop 0
	global_load_lds_dwordx4 v[128:129], off
	s_cbranch_vccnz .LBB0_437
	s_and_b32 s17, s1, 7
	s_cmp_eq_u32 s17, 0
	s_cbranch_scc1 .LBB0_431
	s_lshr_b32 s8, s1, 3
	s_cbranch_execz .LBB0_432
	s_branch .LBB0_436
.LBB0_431:
.LBB0_432:
	s_waitcnt vmcnt(2)
	v_mbcnt_lo_u32_b32 v138, -1, 0
	v_mbcnt_hi_u32_b32 v138, -1, v138
	s_lshr_b32 s8, s1, 3
	s_add_i32 s12, s8, -1
	s_ashr_i32 s13, s12, 31
	s_lshl_b64 s[12:13], s[12:13], s14
	s_add_u32 s12, s50, s12
	s_addc_u32 s13, s51, s13
	s_lshl_b64 s[18:19], s[48:49], 3
	v_and_b32_e32 v137, 7, v138
	v_ashrrev_i32_e32 v136, 3, v138
	v_lshlrev_b32_e32 v146, 2, v138
	s_andn2_b64 vcc, exec, s[54:55]
	v_lshl_add_u32 v147, v137, 10, s66
	v_lshlrev_b32_e32 v148, 2, v136
	v_and_b32_e32 v148, 12, v148
	v_add_u32_e32 v147, 0xc800, v147
	v_add_u32_e32 v147, v147, v148
	v_add_u32_e32 v150, v136, v146
	v_add_u32_e32 v151, 8, v150
	v_add_u32_e32 v152, 16, v150
	v_add_u32_e32 v153, 24, v150
	v_and_b32_e32 v150, 28, v150
	v_and_b32_e32 v151, 28, v151
	v_and_b32_e32 v152, 28, v152
	v_and_b32_e32 v153, 28, v153
	v_lshl_add_u32 v150, v150, 2, v147
	v_lshl_add_u32 v151, v151, 2, v147
	v_lshl_add_u32 v152, v152, 2, v147
	v_lshl_add_u32 v153, v153, 2, v147
	s_cbranch_vccnz .Lfin_nog
	v_lshl_add_u32 v132, v137, 5, s0
	ds_read_b128 v[128:131], v132
	ds_read_b128 v[140:143], v132 offset:16
.Lfin_nog:
	ds_read2_b32 v[188:189], v150 offset0:0 offset1:32
	ds_read2_b32 v[190:191], v150 offset0:64 offset1:96
	ds_read2_b32 v[192:193], v150 offset0:128 offset1:160
	ds_read2_b32 v[194:195], v150 offset0:192 offset1:224
	ds_read2_b32 v[196:197], v151 offset0:0 offset1:32
	ds_read2_b32 v[198:199], v151 offset0:64 offset1:96
	ds_read2_b32 v[200:201], v151 offset0:128 offset1:160
	ds_read2_b32 v[202:203], v151 offset0:192 offset1:224
	s_waitcnt lgkmcnt(7)
	ds_read2_b32 v[204:205], v152 offset0:0 offset1:32
	ds_read2_b32 v[206:207], v152 offset0:64 offset1:96
	ds_read2_b32 v[208:209], v152 offset0:128 offset1:160
	ds_read2_b32 v[210:211], v152 offset0:192 offset1:224
	ds_read2_b32 v[154:155], v153 offset0:0 offset1:32
	ds_read2_b32 v[156:157], v153 offset0:64 offset1:96
	ds_read2_b32 v[158:159], v153 offset0:128 offset1:160
	ds_read2_b32 v[212:213], v153 offset0:192 offset1:224
	v_lshlrev_b32_e32 v166, 3, v137
	v_ashrrev_i32_e32 v137, 31, v136
	s_cbranch_vccnz .Lfin_const
	s_waitcnt lgkmcnt(0)
	v_pk_mul_f32 v[132:133], v[130:131], s[24:25] op_sel_hi:[1,0]
	v_pk_mul_f32 v[134:135], v[128:129], s[24:25] op_sel_hi:[1,0]
	v_pk_mul_f32 v[128:129], v[142:143], s[24:25] op_sel_hi:[1,0]
	v_pk_mul_f32 v[130:131], v[140:141], s[24:25] op_sel_hi:[1,0]
	s_branch .Lfin_go
.Lfin_const:
	v_mov_b32_e32 v130, 0x42800000
	v_mov_b32_e32 v131, 0x42800000
	v_mov_b32_e32 v128, 0x42800000
	v_mov_b32_e32 v129, 0x42800000
	v_mov_b32_e32 v134, 0x42800000
	v_mov_b32_e32 v135, 0x42800000
	v_mov_b32_e32 v132, 0x42800000
	v_mov_b32_e32 v133, 0x42800000
	s_waitcnt lgkmcnt(0)
.Lfin_go:
	v_lshl_add_u64 v[142:143], s[44:45], 0, v[136:137]
	v_mov_b64_e32 v[138:139], s[12:13]
	v_mad_u64_u32 v[144:145], s[12:13], v142, s48, v[138:139]
	v_mul_lo_u32 v139, v142, s49
	v_mul_lo_u32 v142, v143, s48
	v_add3_u32 v145, v142, v145, v139
	v_lshl_add_u64 v[142:143], v[144:145], 0, s[46:47]
	v_lshl_add_u64 v[142:143], v[142:143], 0, v[166:167]
	v_pk_mul_f32 v[188:189], v[188:189], v[134:135]
	v_pk_mul_f32 v[190:191], v[190:191], v[132:133]
	v_pk_mul_f32 v[192:193], v[192:193], v[130:131]
	v_pk_mul_f32 v[194:195], v[194:195], v[128:129]
	v_cvt_pk_fp8_f32 v140, v188, v189
	v_cvt_pk_fp8_f32 v141, v192, v193
	v_cvt_pk_fp8_f32 v140, v190, v191 op_sel:[0,0,1]
	v_cvt_pk_fp8_f32 v141, v194, v195 op_sel:[0,0,1]
	s_nop 1
	global_store_dwordx2 v[142:143], v[140:141], off nt
	v_lshl_add_u64 v[142:143], v[142:143], 0, s[18:19]
	s_nop 0
	v_pk_mul_f32 v[196:197], v[196:197], v[134:135]
	v_pk_mul_f32 v[198:199], v[198:199], v[132:133]
	v_pk_mul_f32 v[200:201], v[200:201], v[130:131]
	v_pk_mul_f32 v[202:203], v[202:203], v[128:129]
	v_cvt_pk_fp8_f32 v140, v196, v197
	v_cvt_pk_fp8_f32 v141, v200, v201
	v_cvt_pk_fp8_f32 v140, v198, v199 op_sel:[0,0,1]
	v_cvt_pk_fp8_f32 v141, v202, v203 op_sel:[0,0,1]
	s_nop 1
	global_store_dwordx2 v[142:143], v[140:141], off nt
	v_lshl_add_u64 v[142:143], v[142:143], 0, s[18:19]
	s_nop 0
	v_pk_mul_f32 v[204:205], v[204:205], v[134:135]
	v_pk_mul_f32 v[206:207], v[206:207], v[132:133]
	v_pk_mul_f32 v[208:209], v[208:209], v[130:131]
	v_pk_mul_f32 v[210:211], v[210:211], v[128:129]
	v_cvt_pk_fp8_f32 v140, v204, v205
	v_cvt_pk_fp8_f32 v141, v208, v209
	v_cvt_pk_fp8_f32 v140, v206, v207 op_sel:[0,0,1]
	v_cvt_pk_fp8_f32 v141, v210, v211 op_sel:[0,0,1]
	s_nop 1
	global_store_dwordx2 v[142:143], v[140:141], off nt
	v_lshl_add_u64 v[142:143], v[142:143], 0, s[18:19]
	s_nop 0
	v_pk_mul_f32 v[154:155], v[154:155], v[134:135]
	v_pk_mul_f32 v[156:157], v[156:157], v[132:133]
	v_pk_mul_f32 v[158:159], v[158:159], v[130:131]
	v_pk_mul_f32 v[212:213], v[212:213], v[128:129]
	v_cvt_pk_fp8_f32 v140, v154, v155
	v_cvt_pk_fp8_f32 v141, v158, v159
	v_cvt_pk_fp8_f32 v140, v156, v157 op_sel:[0,0,1]
	v_cvt_pk_fp8_f32 v141, v212, v213 op_sel:[0,0,1]
	s_nop 1
	global_store_dwordx2 v[142:143], v[140:141], off nt

.LBB0_437:
	s_add_i32 s8, s57, 1
	s_cmp_lg_u32 s57, 2
	s_cselect_b32 s8, s8, 0
	s_add_i32 s12, s15, 1
	s_cmp_lg_u32 s15, 2
	s_cselect_b32 s15, s12, 0
	s_lshl_b32 s12, s15, 13
	s_add_i32 s12, s12, 0
	v_add_u32_e32 v212, s12, v163
	v_add_u32_e32 v213, s12, v220
	v_mfma_scale_f32_32x32x64_f8f6f4 v[144:159], v[228:233], v[182:187], v[80:95], v217, v216 op_sel_hi:[0,0,0] cbsz:2 blgp:2
	v_exp_f32_e32 v96, v96
	v_exp_f32_e32 v97, v97
	v_exp_f32_e32 v98, v98
	v_exp_f32_e32 v99, v99
	v_mfma_scale_f32_32x32x64_f8f6f4 v[128:143], v[234:239], v[182:187], v[80:95], v217, v216 op_sel_hi:[0,0,0] cbsz:2 blgp:2
	v_exp_f32_e32 v100, v100
	v_exp_f32_e32 v101, v101
	v_exp_f32_e32 v102, v102
	v_exp_f32_e32 v103, v103
	v_mfma_scale_f32_32x32x64_f8f6f4 v[144:159], v[240:245], v[176:181], v[144:159], v217, v216 op_sel_hi:[0,0,0] cbsz:2 blgp:2
	v_exp_f32_e32 v104, v104
	v_exp_f32_e32 v105, v105
	v_exp_f32_e32 v106, v106
	v_exp_f32_e32 v107, v107
	v_mfma_scale_f32_32x32x64_f8f6f4 v[128:143], v[246:251], v[176:181], v[128:143], v217, v216 op_sel_hi:[0,0,0] cbsz:2 blgp:2
	s_add_i32 s12, s8, 1
	s_cmp_lg_u32 s8, 2
	s_cselect_b32 s12, s12, 0
	s_lshl_b32 s12, s12, 13
	v_add_u32_e32 v200, s12, v223
	v_add_u32_e32 v201, s12, v224
	v_add_u32_e32 v202, s12, v221
	v_add_u32_e32 v203, s12, v222
	ds_read_b128 v[228:231], v200
	ds_read_b64 v[232:233], v201
	ds_read_b128 v[234:237], v200 offset:4096
	ds_read_b64 v[238:239], v201 offset:4096
	ds_read_b128 v[240:243], v202
	ds_read_b64 v[244:245], v203
	ds_read_b128 v[246:249], v202 offset:4096
	ds_read_b64 v[250:251], v203 offset:4096
	ds_read_b128 v[206:209], v212 offset:24576
	ds_read_b64 v[210:211], v213 offset:24576
	ds_read_b128 v[200:203], v212 offset:26624
	ds_read_b64 v[204:205], v213 offset:26624
	ds_read_b128 v[194:197], v212 offset:28672
	ds_read_b64 v[198:199], v213 offset:28672
	ds_read_b128 v[188:191], v212 offset:30720
	ds_read_b64 v[192:193], v213 offset:30720
	v_exp_f32_e32 v108, v108
	v_exp_f32_e32 v109, v109
	v_exp_f32_e32 v110, v110
	v_exp_f32_e32 v111, v111
	s_nop 0
	v_cvt_scalef32_2xpk16_bf6_f32 v[96:101], v[112:127], v[96:111], 1.0
	s_nop 1
	v_mfma_scale_f32_32x32x64_f8f6f4 v[64:79], v[96:101], v[168:173], v[64:79], v218, v218 op_sel_hi:[0,0,0] cbsz:3 blgp:2
	v_max_f32_e32 v212, v145, v145
	v_max_f32_e32 v213, v144, v144
	v_max_f32_e32 v212, v213, v212
	v_max3_f32 v212, v212, v146, v147
	s_waitcnt lgkmcnt(0)
	v_mfma_scale_f32_32x32x64_f8f6f4 v[0:15], v[96:101], v[206:211], v[0:15], v218, v217 op_sel_hi:[0,0,0] cbsz:3 blgp:2
	v_max3_f32 v212, v212, v148, v149
	v_max3_f32 v212, v212, v150, v151
	v_max3_f32 v212, v212, v152, v153
	v_max3_f32 v212, v212, v154, v155
	v_mfma_scale_f32_32x32x64_f8f6f4 v[48:63], v[96:101], v[200:205], v[48:63], v218, v217 op_sel_hi:[0,0,0] cbsz:3 blgp:2
	v_max3_f32 v212, v212, v156, v157
	v_max3_f32 v212, v212, v158, v159
	v_max3_f32 v212, v212, v128, v129
	v_max3_f32 v212, v212, v130, v131
	v_mfma_scale_f32_32x32x64_f8f6f4 v[32:47], v[96:101], v[194:199], v[32:47], v218, v217 op_sel_hi:[0,0,0] cbsz:3 blgp:2
	v_max3_f32 v212, v212, v132, v133
	v_max3_f32 v212, v212, v134, v135
	v_max3_f32 v212, v212, v136, v137
	v_max3_f32 v212, v212, v138, v139
	v_mfma_scale_f32_32x32x64_f8f6f4 v[16:31], v[96:101], v[188:193], v[16:31], v218, v217 op_sel_hi:[0,0,0] cbsz:3 blgp:2
	v_max3_f32 v212, v212, v140, v141
	v_max3_f32 v212, v212, v142, v143
	v_cmp_ge_f32_e32 vcc, s2, v212
	s_cmp_eq_u64 vcc, exec
	s_cbranch_scc0 .LBB0_445
	s_branch .LBB0_442

.LBB0_444:
	v_mov_b32_e32 v226, v225
	s_nop 1
	v_permlane32_swap_b32_e32 v225, v226
	v_max_f32_e32 v226, v226, v226
	v_max_f32_e32 v225, v225, v225
	v_max_f32_e32 v225, v225, v226
	v_add_f32_e32 v166, -4.0, v225
	v_add_f32_e32 v166, 1.0, v166
	v_max_f32_e32 v226, 0, v166
	v_exp_f32_e64 v166, -v226
	v_pk_add_f32 v[112:113], v[112:113], v[226:227] op_sel_hi:[1,0] neg_lo:[0,1] neg_hi:[0,1]
	v_pk_add_f32 v[114:115], v[114:115], v[226:227] op_sel_hi:[1,0] neg_lo:[0,1] neg_hi:[0,1]
	v_pk_add_f32 v[116:117], v[116:117], v[226:227] op_sel_hi:[1,0] neg_lo:[0,1] neg_hi:[0,1]
	v_pk_add_f32 v[118:119], v[118:119], v[226:227] op_sel_hi:[1,0] neg_lo:[0,1] neg_hi:[0,1]
	v_pk_add_f32 v[120:121], v[120:121], v[226:227] op_sel_hi:[1,0] neg_lo:[0,1] neg_hi:[0,1]
	v_pk_add_f32 v[122:123], v[122:123], v[226:227] op_sel_hi:[1,0] neg_lo:[0,1] neg_hi:[0,1]
	v_pk_add_f32 v[124:125], v[124:125], v[226:227] op_sel_hi:[1,0] neg_lo:[0,1] neg_hi:[0,1]
	v_pk_add_f32 v[126:127], v[126:127], v[226:227] op_sel_hi:[1,0] neg_lo:[0,1] neg_hi:[0,1]
	v_sub_f32_e32 v111, v111, v226
	v_sub_f32_e32 v110, v110, v226
	v_sub_f32_e32 v109, v109, v226
	v_sub_f32_e32 v108, v108, v226
	v_sub_f32_e32 v107, v107, v226
	v_sub_f32_e32 v106, v106, v226
	v_sub_f32_e32 v105, v105, v226
	v_sub_f32_e32 v104, v104, v226
	v_sub_f32_e32 v103, v103, v226
	v_sub_f32_e32 v102, v102, v226
	v_sub_f32_e32 v101, v101, v226
	v_sub_f32_e32 v100, v100, v226
	v_sub_f32_e32 v99, v99, v226
	v_sub_f32_e32 v98, v98, v226
	v_sub_f32_e32 v97, v97, v226
	v_sub_f32_e32 v96, v96, v226
	v_sub_f32_e32 v95, v95, v226
	v_sub_f32_e32 v94, v94, v226
	v_sub_f32_e32 v93, v93, v226
	v_sub_f32_e32 v92, v92, v226
	v_sub_f32_e32 v91, v91, v226
	v_sub_f32_e32 v90, v90, v226
	v_sub_f32_e32 v89, v89, v226
	v_sub_f32_e32 v88, v88, v226
	v_sub_f32_e32 v87, v87, v226
	v_sub_f32_e32 v86, v86, v226
	v_sub_f32_e32 v85, v85, v226
	v_sub_f32_e32 v84, v84, v226
	v_sub_f32_e32 v83, v83, v226
	v_sub_f32_e32 v82, v82, v226
	v_sub_f32_e32 v81, v81, v226
	v_sub_f32_e32 v80, v80, v226
	s_branch .LBB0_420
.LBB0_445:
	v_mov_b32_e32 v213, v212
	s_nop 1
	v_permlane32_swap_b32_e32 v212, v213
	v_max_f32_e32 v213, v213, v213
	v_max_f32_e32 v212, v212, v212
	v_max_f32_e32 v212, v212, v213
	v_add_f32_e32 v166, -4.0, v212
	v_add_f32_e32 v166, 1.0, v166
	v_max_f32_e32 v212, 0, v166
	v_exp_f32_e64 v166, -v212
	v_pk_add_f32 v[144:145], v[144:145], v[212:213] op_sel_hi:[1,0] neg_lo:[0,1] neg_hi:[0,1]
	v_pk_add_f32 v[146:147], v[146:147], v[212:213] op_sel_hi:[1,0] neg_lo:[0,1] neg_hi:[0,1]
	v_pk_add_f32 v[148:149], v[148:149], v[212:213] op_sel_hi:[1,0] neg_lo:[0,1] neg_hi:[0,1]
	v_pk_add_f32 v[150:151], v[150:151], v[212:213] op_sel_hi:[1,0] neg_lo:[0,1] neg_hi:[0,1]
	v_pk_add_f32 v[152:153], v[152:153], v[212:213] op_sel_hi:[1,0] neg_lo:[0,1] neg_hi:[0,1]
	v_pk_add_f32 v[154:155], v[154:155], v[212:213] op_sel_hi:[1,0] neg_lo:[0,1] neg_hi:[0,1]
	v_pk_add_f32 v[156:157], v[156:157], v[212:213] op_sel_hi:[1,0] neg_lo:[0,1] neg_hi:[0,1]
	v_pk_add_f32 v[158:159], v[158:159], v[212:213] op_sel_hi:[1,0] neg_lo:[0,1] neg_hi:[0,1]
	v_sub_f32_e32 v143, v143, v212
	v_sub_f32_e32 v142, v142, v212
	v_sub_f32_e32 v141, v141, v212
	v_sub_f32_e32 v140, v140, v212
	v_sub_f32_e32 v139, v139, v212
	v_sub_f32_e32 v138, v138, v212
	v_sub_f32_e32 v137, v137, v212
	v_sub_f32_e32 v136, v136, v212
	v_sub_f32_e32 v135, v135, v212
	v_sub_f32_e32 v134, v134, v212
	v_sub_f32_e32 v133, v133, v212
	v_sub_f32_e32 v132, v132, v212
	v_sub_f32_e32 v131, v131, v212
	v_sub_f32_e32 v130, v130, v212
	v_sub_f32_e32 v129, v129, v212
	v_sub_f32_e32 v128, v128, v212
	v_sub_f32_e32 v95, v95, v212
	v_sub_f32_e32 v94, v94, v212
	v_sub_f32_e32 v93, v93, v212
	v_sub_f32_e32 v92, v92, v212
	v_sub_f32_e32 v91, v91, v212
	v_sub_f32_e32 v90, v90, v212
	v_sub_f32_e32 v89, v89, v212
	v_sub_f32_e32 v88, v88, v212
	v_sub_f32_e32 v87, v87, v212
	v_sub_f32_e32 v86, v86, v212
	v_sub_f32_e32 v85, v85, v212
	v_sub_f32_e32 v84, v84, v212
	v_sub_f32_e32 v83, v83, v212
	v_sub_f32_e32 v82, v82, v212
	v_sub_f32_e32 v81, v81, v212
	v_sub_f32_e32 v80, v80, v212
	s_branch .LBB0_438

.LBB0_452:
	v_mov_b32_e32 v164, 1.0
	s_waitcnt lgkmcnt(0)
	v_mfma_scale_f32_32x32x64_f8f6f4 v[96:111], v[228:233], v[182:187], v[80:95], v217, v216 op_sel_hi:[0,0,0] cbsz:2 blgp:2
	v_mfma_scale_f32_32x32x64_f8f6f4 v[80:95], v[234:239], v[182:187], v[80:95], v217, v216 op_sel_hi:[0,0,0] cbsz:2 blgp:2
	v_mfma_scale_f32_32x32x64_f8f6f4 v[96:111], v[240:245], v[176:181], v[96:111], v217, v216 op_sel_hi:[0,0,0] cbsz:2 blgp:2
	v_mfma_scale_f32_32x32x64_f8f6f4 v[80:95], v[246:251], v[176:181], v[80:95], v217, v216 op_sel_hi:[0,0,0] cbsz:2 blgp:2
	s_lshl_b32 s1, s15, 13
	s_add_i32 s8, s1, 0
	v_add_u32_e32 v112, s8, v163
	v_add_u32_e32 v113, s8, v220
	ds_read_b128 v[192:195], v112 offset:24576
	ds_read_b64 v[196:197], v113 offset:24576
	ds_read_b128 v[186:189], v112 offset:26624
	ds_read_b64 v[190:191], v113 offset:26624
	ds_read_b128 v[180:183], v112 offset:28672
	ds_read_b64 v[184:185], v113 offset:28672
	ds_read_b128 v[174:177], v112 offset:30720
	ds_read_b64 v[178:179], v113 offset:30720
	v_max_f32_e32 v112, v97, v97
	v_max_f32_e32 v113, v96, v96
	v_max_f32_e32 v112, v113, v112
	v_max3_f32 v112, v112, v98, v99
	v_max3_f32 v112, v112, v100, v101
	v_max3_f32 v112, v112, v102, v103
	v_max3_f32 v112, v112, v104, v105
	v_max3_f32 v112, v112, v106, v107
	v_max3_f32 v112, v112, v108, v109
	v_max3_f32 v112, v112, v110, v111
	v_max3_f32 v112, v112, v80, v81
	v_max3_f32 v112, v112, v82, v83
	v_max3_f32 v112, v112, v84, v85
	v_max3_f32 v112, v112, v86, v87
	v_max3_f32 v112, v112, v88, v89
	v_max3_f32 v112, v112, v90, v91
	v_max3_f32 v112, v112, v92, v93
	v_max3_f32 v112, v112, v94, v95
	v_mov_b32_e32 v113, v112
	s_nop 1
	v_permlane32_swap_b32_e32 v112, v113
	v_max_f32_e32 v113, v113, v113
	v_max_f32_e32 v112, v112, v112
	v_max_f32_e32 v112, v112, v113
	v_cmp_ge_f32_e32 vcc, s2, v112
	s_cmp_eq_u64 vcc, exec
	s_cbranch_scc0 .LBB0_460

.LBB0_469:
	v_lshl_add_u64 v[66:67], v[154:155], 0, s[96:97]
	v_add_co_u32_e32 v70, vcc, 0x52002000, v66
	v_lshl_add_u64 v[68:69], v[156:157], 0, s[96:97]
	s_nop 0
	v_addc_co_u32_e32 v71, vcc, 0, v67, vcc
	global_load_dwordx2 v[164:165], v[70:71], off
	v_add_co_u32_e32 v70, vcc, 0x52002000, v68
	s_and_b32 s1, s3, 0x4000
	s_nop 0
	v_addc_co_u32_e32 v71, vcc, 0, v69, vcc
	v_add_co_u32_e32 v66, vcc, 0x4e002000, v66
	global_load_dwordx2 v[162:163], v[70:71], off
	s_nop 0
	v_addc_co_u32_e32 v67, vcc, 0, v67, vcc
	global_load_dwordx2 v[160:161], v[66:67], off
	v_add_co_u32_e32 v66, vcc, 0x4e002000, v68
	s_add_i32 s72, s1, 0
	s_nop 0
	v_addc_co_u32_e32 v67, vcc, 0, v69, vcc
	v_add3_u32 v0, s72, v199, v189
	v_add3_u32 v98, s72, v197, v189
	global_load_dwordx2 v[158:159], v[66:67], off
	ds_read_b128 v[66:69], v0 offset:32768
	ds_read_b128 v[98:101], v98 offset:32768
	v_add_u32_e32 v0, s72, v189
	v_add_u32_e32 v70, v0, v199
	ds_read_b128 v[70:73], v70 offset:40960
	v_add_u32_e32 v102, v0, v197
	ds_read_b128 v[102:105], v102 offset:40960
	s_waitcnt lgkmcnt(3)
	v_mfma_f32_32x32x16_bf16 v[82:97], v[66:69], v[114:117], 0
	s_cmp_lt_u32 s92, s84
	s_waitcnt lgkmcnt(1)
	v_mfma_f32_32x32x16_bf16 v[66:81], v[70:73], v[114:117], 0
	s_waitcnt lgkmcnt(0)
	v_mfma_f32_32x32x16_bf16 v[66:81], v[102:105], v[118:121], v[66:81]
	v_add_u32_e32 v102, v0, v195
	ds_read_b128 v[102:105], v102 offset:40960
	s_waitcnt lgkmcnt(0)
	v_mfma_f32_32x32x16_bf16 v[66:81], v[102:105], v[122:125], v[66:81]
	v_add_u32_e32 v102, v0, v194
	ds_read_b128 v[102:105], v102 offset:40960
	s_waitcnt lgkmcnt(0)
	v_mfma_f32_32x32x16_bf16 v[66:81], v[102:105], v[126:129], v[66:81]
	v_add_u32_e32 v102, v0, v193
	ds_read_b128 v[102:105], v102 offset:40960
	s_waitcnt lgkmcnt(0)
	v_mfma_f32_32x32x16_bf16 v[66:81], v[102:105], v[130:133], v[66:81]
	v_add_u32_e32 v102, v0, v192
	ds_read_b128 v[102:105], v102 offset:40960
	v_mfma_f32_32x32x16_bf16 v[82:97], v[98:101], v[118:121], v[82:97]
	v_add3_u32 v98, s72, v195, v189
	ds_read_b128 v[98:101], v98 offset:32768
	s_waitcnt lgkmcnt(1)
	v_mfma_f32_32x32x16_bf16 v[66:81], v[102:105], v[134:137], v[66:81]
	v_add_u32_e32 v102, v0, v191
	ds_read_b128 v[102:105], v102 offset:40960
	v_add_u32_e32 v0, v0, v190
	s_waitcnt lgkmcnt(0)
	v_mfma_f32_32x32x16_bf16 v[66:81], v[102:105], v[138:141], v[66:81]
	ds_read_b128 v[102:105], v0 offset:40960
	v_mfma_f32_32x32x16_bf16 v[82:97], v[98:101], v[122:125], v[82:97]
	v_add3_u32 v98, s72, v194, v189
	ds_read_b128 v[98:101], v98 offset:32768
	s_waitcnt lgkmcnt(0)
	v_mfma_f32_32x32x16_bf16 v[82:97], v[98:101], v[126:129], v[82:97]
	v_add3_u32 v98, s72, v193, v189
	ds_read_b128 v[98:101], v98 offset:32768
	s_waitcnt lgkmcnt(0)
	v_mfma_f32_32x32x16_bf16 v[82:97], v[98:101], v[130:133], v[82:97]
	v_add3_u32 v98, s72, v192, v189
	ds_read_b128 v[98:101], v98 offset:32768
	s_waitcnt lgkmcnt(0)
	v_mfma_f32_32x32x16_bf16 v[82:97], v[98:101], v[134:137], v[82:97]
	v_add3_u32 v98, s72, v191, v189
	ds_read_b128 v[98:101], v98 offset:32768
	s_waitcnt lgkmcnt(0)
	v_mfma_f32_32x32x16_bf16 v[82:97], v[98:101], v[138:141], v[82:97]
	v_add3_u32 v98, s72, v190, v189
	ds_read_b128 v[98:101], v98 offset:32768
	s_cselect_b64 s[72:73], -1, 0
	s_cmp_ge_u32 s92, s88
	s_cselect_b64 s[86:87], -1, 0
	s_or_b64 s[86:87], s[72:73], s[86:87]
	s_mov_b64 s[72:73], -1
	s_waitcnt lgkmcnt(0)
	s_add_i32 s72, s2, s92
	v_med3_i32 v239, s72, -7, 7
	v_lshlrev_b32_e32 v239, 7, v239
	v_lshl_add_u32 v239, v183, 2, v239
	v_add_u32_e32 v239, 0x10bbc, v239
	ds_read2_b32 v[206:207], v239 offset0:0 offset1:32
	ds_read2_b32 v[208:209], v239 offset0:1 offset1:33
	ds_read2_b32 v[210:211], v239 offset0:2 offset1:34
	ds_read2_b32 v[212:213], v239 offset0:3 offset1:35
	ds_read2_b32 v[214:215], v239 offset0:8 offset1:40
	ds_read2_b32 v[216:217], v239 offset0:9 offset1:41
	ds_read2_b32 v[218:219], v239 offset0:10 offset1:42
	ds_read2_b32 v[220:221], v239 offset0:11 offset1:43
	ds_read2_b32 v[222:223], v239 offset0:16 offset1:48
	ds_read2_b32 v[224:225], v239 offset0:17 offset1:49
	ds_read2_b32 v[226:227], v239 offset0:18 offset1:50
	ds_read2_b32 v[228:229], v239 offset0:19 offset1:51
	ds_read2_b32 v[230:231], v239 offset0:24 offset1:56
	ds_read2_b32 v[232:233], v239 offset0:25 offset1:57
	ds_read2_b32 v[234:235], v239 offset0:26 offset1:58
	ds_read2_b32 v[236:237], v239 offset0:27 offset1:59
	v_mfma_f32_32x32x16_bf16 v[82:97], v[98:101], v[142:145], v[82:97]
	s_and_b64 vcc, exec, s[86:87]
	v_mfma_f32_32x32x16_bf16 v[66:81], v[102:105], v[142:145], v[66:81]
	v_mov_b32_e32 v238, 0xff800000
	s_nop 11
	s_cbranch_vccnz .Lna_inv
	s_waitcnt lgkmcnt(0)
	v_add_f32_e32 v206, v82, v206
	v_add_f32_e32 v207, v66, v207
	v_cndmask_b32_e64 v82, v238, v206, s[70:71]
	v_cndmask_b32_e64 v0, v238, v207, s[68:69]
	v_add_f32_e32 v208, v83, v208
	v_add_f32_e32 v209, v67, v209
	v_cndmask_b32_e64 v83, v238, v208, s[66:67]
	v_cndmask_b32_e64 v66, v238, v209, s[64:65]
	v_add_f32_e32 v210, v84, v210
	v_add_f32_e32 v211, v68, v211
	v_cndmask_b32_e64 v84, v238, v210, s[62:63]
	v_cndmask_b32_e64 v67, v238, v211, s[60:61]
	v_add_f32_e32 v212, v85, v212
	v_add_f32_e32 v213, v69, v213
	v_cndmask_b32_e64 v85, v238, v212, s[58:59]
	v_cndmask_b32_e64 v68, v238, v213, s[56:57]
	v_add_f32_e32 v214, v86, v214
	v_add_f32_e32 v215, v70, v215
	v_cndmask_b32_e64 v86, v238, v214, s[54:55]
	v_cndmask_b32_e64 v69, v238, v215, s[52:53]
	v_add_f32_e32 v216, v87, v216
	v_add_f32_e32 v217, v71, v217
	v_cndmask_b32_e64 v87, v238, v216, s[50:51]
	v_cndmask_b32_e64 v70, v238, v217, s[48:49]
	v_add_f32_e32 v218, v88, v218
	v_add_f32_e32 v219, v72, v219
	v_cndmask_b32_e64 v88, v238, v218, s[46:47]
	v_cndmask_b32_e64 v71, v238, v219, s[44:45]
	v_add_f32_e32 v220, v89, v220
	v_add_f32_e32 v221, v73, v221
	v_cndmask_b32_e64 v89, v238, v220, s[42:43]
	v_cndmask_b32_e64 v72, v238, v221, s[40:41]
	v_add_f32_e32 v222, v90, v222
	v_add_f32_e32 v223, v74, v223
	v_cndmask_b32_e64 v90, v238, v222, s[38:39]
	v_cndmask_b32_e64 v73, v238, v223, s[36:37]
	v_add_f32_e32 v224, v91, v224
	v_add_f32_e32 v225, v75, v225
	v_cndmask_b32_e64 v91, v238, v224, s[34:35]
	v_cndmask_b32_e64 v74, v238, v225, s[30:31]
	v_add_f32_e32 v226, v92, v226
	v_add_f32_e32 v227, v76, v227
	v_cndmask_b32_e64 v92, v238, v226, s[28:29]
	v_cndmask_b32_e64 v75, v238, v227, s[26:27]
	v_add_f32_e32 v228, v93, v228
	v_add_f32_e32 v229, v77, v229
	v_cndmask_b32_e64 v93, v238, v228, s[24:25]
	v_cndmask_b32_e64 v76, v238, v229, s[22:23]
	v_add_f32_e32 v230, v94, v230
	v_add_f32_e32 v231, v78, v231
	v_cndmask_b32_e64 v94, v238, v230, s[20:21]
	v_cndmask_b32_e64 v77, v238, v231, s[18:19]
	v_add_f32_e32 v232, v95, v232
	v_add_f32_e32 v233, v79, v233
	v_cndmask_b32_e64 v95, v238, v232, s[16:17]
	v_cndmask_b32_e64 v78, v238, v233, s[14:15]
	v_add_f32_e32 v234, v96, v234
	v_add_f32_e32 v235, v80, v235
	v_cndmask_b32_e64 v96, v238, v234, s[12:13]
	v_cndmask_b32_e64 v79, v238, v235, s[10:11]
	v_add_f32_e32 v236, v97, v236
	v_add_f32_e32 v237, v81, v237
	v_cndmask_b32_e64 v97, v238, v236, s[8:9]
	v_cndmask_b32_e64 v80, v238, v237, s[6:7]
	s_branch .LBB0_597
.Lna_inv:
	v_mov_b32_e32 v82, v238
	v_mov_b32_e32 v83, v238
	v_mov_b32_e32 v84, v238
	v_mov_b32_e32 v85, v238
	v_mov_b32_e32 v86, v238
	v_mov_b32_e32 v87, v238
	v_mov_b32_e32 v88, v238
	v_mov_b32_e32 v89, v238
	v_mov_b32_e32 v90, v238
	v_mov_b32_e32 v91, v238
	v_mov_b32_e32 v92, v238
	v_mov_b32_e32 v93, v238
	v_mov_b32_e32 v94, v238
	v_mov_b32_e32 v95, v238
	v_mov_b32_e32 v96, v238
	v_mov_b32_e32 v97, v238
	v_mov_b32_e32 v0, v238
	v_mov_b32_e32 v66, v238
	v_mov_b32_e32 v67, v238
	v_mov_b32_e32 v68, v238
	v_mov_b32_e32 v69, v238
	v_mov_b32_e32 v70, v238
	v_mov_b32_e32 v71, v238
	v_mov_b32_e32 v72, v238
	v_mov_b32_e32 v73, v238
	v_mov_b32_e32 v74, v238
	v_mov_b32_e32 v75, v238
	v_mov_b32_e32 v76, v238
	v_mov_b32_e32 v77, v238
	v_mov_b32_e32 v78, v238
	v_mov_b32_e32 v79, v238
	v_mov_b32_e32 v80, v238
	s_waitcnt lgkmcnt(0)
